# w_in GEMM phase: 184 GEMM workgroups (18 rounds of units instead of 19) and 72 conversion workgroups
# baseline (speedup 1.0000x reference)
; __device__ __forceinline__ int xcd_remap(int L, int nwg) { const int q = nwg / NXCD, r = nwg % NXCD, xcd = L % NXCD, off = L / NXCD; return (xcd < r ? xcd * (q + 1) : r * (q + 1) + (xcd - r) * q) + off; }
; #define PHASE(k, ...) do { if (IN(k)) { __VA_ARGS__ if ((REP_MASK >> (k)) & 1) { GRID_BAR(); __VA_ARGS__ } } SEAM(k); } while (0)
;     DI bool next(int i, pg8::Unit& u) const {
;         const int L = i * G + c; if (L >= 3200 + 14) return false;
;         int pm, pn;
;         if (L < 3200) pg8::tile_order(pg8::xcd_remap(L, 3200), 3200, 128, 25, pm, pn);
;         else { const int j = L - 3200; pm = 128 + j / 7; pn = (j % 7) < 6 ? 2 + (j % 7) : 24; }
;         const unsigned xrow = (unsigned)(WS_XN + (size_t)pm * 256 * D), wrow = (unsigned)(WS_WIN + (size_t)pn * 256 * D);
; __global__ void __launch_bounds__(512, 2) hymba_fwd(Params P) {
;     ...
;     PHASE(2, { const int ng = slots ? NG_IN : G;
;                if (bid < ng) { SchedIn S{P.ws, ng, bid}; pg8::EpiStore E{P.in[I_BIF], (const float*)(P.ws + WS_XSC), (const float*)(P.ws + WS_WSC)}; pg8::gemm_phase<pg8::EpiStore, SchedIn, true, true, 2>(lds, P.ws, D, S, E); }
;                if (slots) conv_pool(P, lds, 0, 0, CV_NBLK_A); });
.LBB0_268:
	v_readlane_b32 s2, v254, 16
	v_readlane_b32 s3, v254, 17
	s_cmp_lt_i32 s2, 3
	s_cselect_b64 s[2:3], -1, 0
	s_and_b64 s[8:9], s[2:3], s[0:1]
	s_andn2_b64 vcc, exec, s[8:9]
	s_cbranch_vccnz .LBB0_383
	s_and_b64 s[0:1], s[88:89], exec
	v_readlane_b32 s0, v254, 18
	v_readlane_b32 s1, v254, 19
	s_cselect_b32 s33, 0xb8, s0
	v_readlane_b32 s0, v254, 0
	s_cmp_ge_i32 s0, s33
	v_readlane_b32 s1, v254, 1
	s_cbranch_scc1 .LBB0_358
	s_getreg_b32 s0, hwreg(HW_REG_HW_ID, 0, 6)
	s_and_b32 s0, s0, 63
	s_lshl_b32 s0, s0, 2
	s_add_i32 s0, s0, 0
	s_add_i32 s0, s0, 0x24400
	v_mov_b32_e32 v0, s0
	ds_read_b32 v1, v0
	v_readlane_b32 s4, v254, 0
	s_cmpk_lt_i32 s4, 0xc8e
	v_mbcnt_lo_u32_b32 v0, -1, 0
	v_mbcnt_hi_u32_b32 v0, -1, v0
	s_cselect_b64 s[0:1], -1, 0
	s_waitcnt lgkmcnt(0)
	v_readfirstlane_b32 s2, v1
	s_cmpk_gt_i32 s4, 0xc8d
	v_readlane_b32 s5, v254, 1
	v_lshl_add_u32 v1, s2, 6, v0
	s_nop 0
	v_readfirstlane_b32 s12, v1
	s_cbranch_scc1 .LBB0_273
	s_cmpk_gt_i32 s4, 0xc7f
	s_cbranch_scc0 .LBB0_274
	s_add_i32 s2, s4, 0xfffff380
	s_cmp_gt_u32 s2, 6
	s_movk_i32 s3, 0x81
	s_cselect_b32 s52, s3, 0x80
	s_add_i32 s3, s4, 0xfffff379
	s_cmp_lt_u32 s2, 7
	s_cselect_b32 s2, s2, s3
	s_add_i32 s3, s2, 2
	s_cmp_lt_u32 s2, 6
	s_cselect_b32 s83, s3, 24
	s_cbranch_execz .LBB0_275
	s_branch .LBB0_276
